# all conformer-conv de-serialisations together: both tap ladders pipelined, permlane-swap reductions, pre-loop wait moved to its consumer
# baseline (speedup 1.0000x reference)
.LBB0_2165:
	ds_read_u16 v29, v22
	ds_read_u16 v30, v22 offset:1024
	ds_read_u16 v31, v22 offset:2048
	ds_read_u16 v32, v22 offset:3072
	ds_read_u16 v33, v22 offset:4096
	ds_read_u16 v34, v22 offset:5120
	ds_read_u16 v35, v22 offset:6144
	ds_read_u16 v36, v22 offset:7168
	s_waitcnt lgkmcnt(7)
	v_lshlrev_b32_e32 v29, 16, v29
	v_fma_f32 v29, v51, v29, v52
	s_waitcnt lgkmcnt(6)
	v_lshlrev_b32_e32 v30, 16, v30
	v_fmac_f32_e32 v29, v54, v30
	v_fma_f32 v30, v51, v30, v52
	s_waitcnt lgkmcnt(5)
	v_lshlrev_b32_e32 v31, 16, v31
	v_fmac_f32_e32 v29, v55, v31
	v_fmac_f32_e32 v30, v54, v31
	v_fma_f32 v31, v51, v31, v52
	s_waitcnt lgkmcnt(4)
	v_lshlrev_b32_e32 v32, 16, v32
	ds_read_u16 v37, v22 offset:8192
	ds_read_u16 v38, v22 offset:9216
	ds_read_u16 v39, v22 offset:10240
	ds_read_u16 v40, v22 offset:11264
	ds_read_u16 v41, v22 offset:12288
	ds_read_u16 v42, v22 offset:13312
	ds_read_u16 v43, v22 offset:14336
	ds_read_u16 v44, v22 offset:15360
	v_fmac_f32_e32 v29, v56, v32
	v_fmac_f32_e32 v30, v55, v32
	v_fmac_f32_e32 v31, v54, v32
	v_fma_f32 v32, v51, v32, v52
	s_waitcnt lgkmcnt(11)
	v_lshlrev_b32_e32 v33, 16, v33
	v_fmac_f32_e32 v29, v57, v33
	v_fmac_f32_e32 v30, v56, v33
	v_fmac_f32_e32 v31, v55, v33
	v_fmac_f32_e32 v32, v54, v33
	v_fma_f32 v33, v51, v33, v52
	s_waitcnt lgkmcnt(10)
	v_lshlrev_b32_e32 v34, 16, v34
	v_fmac_f32_e32 v29, v58, v34
	v_fmac_f32_e32 v30, v57, v34
	v_fmac_f32_e32 v31, v56, v34
	v_fmac_f32_e32 v32, v55, v34
	v_fmac_f32_e32 v33, v54, v34
	v_fma_f32 v34, v51, v34, v52
	s_waitcnt lgkmcnt(9)
	v_lshlrev_b32_e32 v35, 16, v35
	v_fmac_f32_e32 v29, v59, v35
	v_fmac_f32_e32 v30, v58, v35
	v_fmac_f32_e32 v31, v57, v35
	v_fmac_f32_e32 v32, v56, v35
	v_fmac_f32_e32 v33, v55, v35
	v_fmac_f32_e32 v34, v54, v35
	v_fma_f32 v35, v51, v35, v52
	s_waitcnt lgkmcnt(8)
	v_lshlrev_b32_e32 v36, 16, v36
	v_fmac_f32_e32 v29, v60, v36
	v_fmac_f32_e32 v30, v59, v36
	v_fmac_f32_e32 v31, v58, v36
	v_fmac_f32_e32 v32, v57, v36
	v_fmac_f32_e32 v33, v56, v36
	v_fmac_f32_e32 v34, v55, v36
	v_fmac_f32_e32 v35, v54, v36
	v_fma_f32 v36, v51, v36, v52
	s_waitcnt lgkmcnt(7)
	v_lshlrev_b32_e32 v37, 16, v37
	v_fmac_f32_e32 v29, v61, v37
	v_fmac_f32_e32 v30, v60, v37
	v_fmac_f32_e32 v31, v59, v37
	v_fmac_f32_e32 v32, v58, v37
	v_fmac_f32_e32 v33, v57, v37
	v_fmac_f32_e32 v34, v56, v37
	v_fmac_f32_e32 v35, v55, v37
	v_fmac_f32_e32 v36, v54, v37
	v_fma_f32 v37, v51, v37, v52
	s_waitcnt lgkmcnt(6)
	v_lshlrev_b32_e32 v38, 16, v38
	v_fmac_f32_e32 v29, v62, v38
	v_fmac_f32_e32 v30, v61, v38
	v_fmac_f32_e32 v31, v60, v38
	v_fmac_f32_e32 v32, v59, v38
	v_fmac_f32_e32 v33, v58, v38
	v_fmac_f32_e32 v34, v57, v38
	v_fmac_f32_e32 v35, v56, v38
	v_fmac_f32_e32 v36, v55, v38
	v_fmac_f32_e32 v37, v54, v38
	v_fma_f32 v38, v51, v38, v52
	s_waitcnt lgkmcnt(5)
	v_lshlrev_b32_e32 v39, 16, v39
	v_fmac_f32_e32 v29, v63, v39
	v_fmac_f32_e32 v30, v62, v39
	v_fmac_f32_e32 v31, v61, v39
	v_fmac_f32_e32 v32, v60, v39
	v_fmac_f32_e32 v33, v59, v39
	v_fmac_f32_e32 v34, v58, v39
	v_fmac_f32_e32 v35, v57, v39
	v_fmac_f32_e32 v36, v56, v39
	v_fmac_f32_e32 v37, v55, v39
	v_fmac_f32_e32 v38, v54, v39
	v_fma_f32 v39, v51, v39, v52
	s_waitcnt lgkmcnt(4)
	v_lshlrev_b32_e32 v40, 16, v40
	ds_read_u16 v45, v22 offset:16384
	v_fmac_f32_e32 v29, v64, v40
	v_fmac_f32_e32 v30, v63, v40
	v_fmac_f32_e32 v31, v62, v40
	v_fmac_f32_e32 v32, v61, v40
	v_fmac_f32_e32 v33, v60, v40
	v_fmac_f32_e32 v34, v59, v40
	v_fmac_f32_e32 v35, v58, v40
	v_fmac_f32_e32 v36, v57, v40
	v_fmac_f32_e32 v37, v56, v40
	v_fmac_f32_e32 v38, v55, v40
	v_fmac_f32_e32 v39, v54, v40
	v_fma_f32 v40, v51, v40, v52
	s_waitcnt lgkmcnt(4)
	v_lshlrev_b32_e32 v41, 16, v41
	v_fmac_f32_e32 v29, v65, v41
	v_fmac_f32_e32 v30, v64, v41
	v_fmac_f32_e32 v31, v63, v41
	v_fmac_f32_e32 v32, v62, v41
	v_fmac_f32_e32 v33, v61, v41
	v_fmac_f32_e32 v34, v60, v41
	v_fmac_f32_e32 v35, v59, v41
	v_fmac_f32_e32 v36, v58, v41
	v_fmac_f32_e32 v37, v57, v41
	v_fmac_f32_e32 v38, v56, v41
	v_fmac_f32_e32 v39, v55, v41
	v_fmac_f32_e32 v40, v54, v41
	v_fma_f32 v41, v51, v41, v52
	s_waitcnt lgkmcnt(3)
	v_lshlrev_b32_e32 v42, 16, v42
	v_fmac_f32_e32 v29, v66, v42
	v_fmac_f32_e32 v30, v65, v42
	v_fmac_f32_e32 v31, v64, v42
	v_fmac_f32_e32 v32, v63, v42
	v_fmac_f32_e32 v33, v62, v42
	v_fmac_f32_e32 v34, v61, v42
	v_fmac_f32_e32 v35, v60, v42
	v_fmac_f32_e32 v36, v59, v42
	v_fmac_f32_e32 v37, v58, v42
	v_fmac_f32_e32 v38, v57, v42
	v_fmac_f32_e32 v39, v56, v42
	v_fmac_f32_e32 v40, v55, v42
	v_fmac_f32_e32 v41, v54, v42
	v_fma_f32 v42, v51, v42, v52
	s_waitcnt lgkmcnt(2)
	v_lshlrev_b32_e32 v43, 16, v43
	v_fmac_f32_e32 v29, v67, v43
	v_fmac_f32_e32 v30, v66, v43
	v_fmac_f32_e32 v31, v65, v43
	v_fmac_f32_e32 v32, v64, v43
	v_fmac_f32_e32 v33, v63, v43
	v_fmac_f32_e32 v34, v62, v43
	v_fmac_f32_e32 v35, v61, v43
	v_fmac_f32_e32 v36, v60, v43
	v_fmac_f32_e32 v37, v59, v43
	v_fmac_f32_e32 v38, v58, v43
	v_fmac_f32_e32 v39, v57, v43
	v_fmac_f32_e32 v40, v56, v43
	v_fmac_f32_e32 v41, v55, v43
	v_fmac_f32_e32 v42, v54, v43
	v_fma_f32 v43, v51, v43, v52
	s_waitcnt lgkmcnt(1)
	v_lshlrev_b32_e32 v44, 16, v44
	v_fmac_f32_e32 v29, v68, v44
	v_fmac_f32_e32 v30, v67, v44
	v_fmac_f32_e32 v31, v66, v44
	v_fmac_f32_e32 v32, v65, v44
	v_fmac_f32_e32 v33, v64, v44
	v_fmac_f32_e32 v34, v63, v44
	v_fmac_f32_e32 v35, v62, v44
	v_fmac_f32_e32 v36, v61, v44
	v_fmac_f32_e32 v37, v60, v44
	v_fmac_f32_e32 v38, v59, v44
	v_fmac_f32_e32 v39, v58, v44
	v_fmac_f32_e32 v40, v57, v44
	v_fmac_f32_e32 v41, v56, v44
	v_fmac_f32_e32 v42, v55, v44
	v_fmac_f32_e32 v43, v54, v44
	v_fma_f32 v44, v51, v44, v52
	s_waitcnt lgkmcnt(0)
	v_lshlrev_b32_e32 v45, 16, v45
	v_fmac_f32_e32 v29, v69, v45
	v_fmac_f32_e32 v30, v68, v45
	v_fmac_f32_e32 v31, v67, v45
	v_fmac_f32_e32 v32, v66, v45
	v_fmac_f32_e32 v33, v65, v45
	v_fmac_f32_e32 v34, v64, v45
	v_fmac_f32_e32 v35, v63, v45
	v_fmac_f32_e32 v36, v62, v45
	v_fmac_f32_e32 v37, v61, v45
	v_fmac_f32_e32 v38, v60, v45
	v_fmac_f32_e32 v39, v59, v45
	v_fmac_f32_e32 v40, v58, v45
	v_fmac_f32_e32 v41, v57, v45
	v_fmac_f32_e32 v42, v56, v45
	v_fmac_f32_e32 v43, v55, v45
	v_fmac_f32_e32 v44, v54, v45
	ds_read_u16 v100, v22 offset:17408
	ds_read_u16 v101, v22 offset:18432
	ds_read_u16 v102, v22 offset:19456
	ds_read_u16 v103, v22 offset:20480
	ds_read_u16 v104, v22 offset:21504
	ds_read_u16 v105, v22 offset:22528
	ds_read_u16 v106, v22 offset:23552
	ds_read_u16 v107, v22 offset:24576
	s_waitcnt lgkmcnt(7)
	v_lshlrev_b32_e32 v45, 16, v100
	ds_read_u16 v100, v22 offset:25600
	v_fmac_f32_e32 v29, v70, v45
	v_fmac_f32_e32 v30, v69, v45
	v_fmac_f32_e32 v31, v68, v45
	v_fmac_f32_e32 v32, v67, v45
	v_fmac_f32_e32 v33, v66, v45
	v_fmac_f32_e32 v34, v65, v45
	v_fmac_f32_e32 v35, v64, v45
	v_fmac_f32_e32 v36, v63, v45
	v_fmac_f32_e32 v37, v62, v45
	v_fmac_f32_e32 v38, v61, v45
	v_fmac_f32_e32 v39, v60, v45
	v_fmac_f32_e32 v40, v59, v45
	v_fmac_f32_e32 v41, v58, v45
	v_fmac_f32_e32 v42, v57, v45
	v_fmac_f32_e32 v43, v56, v45
	v_fmac_f32_e32 v44, v55, v45
	s_waitcnt lgkmcnt(7)
	v_lshlrev_b32_e32 v45, 16, v101
	ds_read_u16 v101, v22 offset:26624
	v_fmac_f32_e32 v29, v71, v45
	v_fmac_f32_e32 v30, v70, v45
	v_fmac_f32_e32 v31, v69, v45
	v_fmac_f32_e32 v32, v68, v45
	v_fmac_f32_e32 v33, v67, v45
	v_fmac_f32_e32 v34, v66, v45
	v_fmac_f32_e32 v35, v65, v45
	v_fmac_f32_e32 v36, v64, v45
	v_fmac_f32_e32 v37, v63, v45
	v_fmac_f32_e32 v38, v62, v45
	v_fmac_f32_e32 v39, v61, v45
	v_fmac_f32_e32 v40, v60, v45
	v_fmac_f32_e32 v41, v59, v45
	v_fmac_f32_e32 v42, v58, v45
	v_fmac_f32_e32 v43, v57, v45
	v_fmac_f32_e32 v44, v56, v45
	s_waitcnt lgkmcnt(7)
	v_lshlrev_b32_e32 v45, 16, v102
	ds_read_u16 v102, v22 offset:27648
	v_fmac_f32_e32 v29, v72, v45
	v_fmac_f32_e32 v30, v71, v45
	v_fmac_f32_e32 v31, v70, v45
	v_fmac_f32_e32 v32, v69, v45
	v_fmac_f32_e32 v33, v68, v45
	v_fmac_f32_e32 v34, v67, v45
	v_fmac_f32_e32 v35, v66, v45
	v_fmac_f32_e32 v36, v65, v45
	v_fmac_f32_e32 v37, v64, v45
	v_fmac_f32_e32 v38, v63, v45
	v_fmac_f32_e32 v39, v62, v45
	v_fmac_f32_e32 v40, v61, v45
	v_fmac_f32_e32 v41, v60, v45
	v_fmac_f32_e32 v42, v59, v45
	v_fmac_f32_e32 v43, v58, v45
	v_fmac_f32_e32 v44, v57, v45
	s_waitcnt lgkmcnt(7)
	v_lshlrev_b32_e32 v45, 16, v103
	ds_read_u16 v103, v22 offset:28672
	v_fmac_f32_e32 v29, v73, v45
	v_fmac_f32_e32 v30, v72, v45
	v_fmac_f32_e32 v31, v71, v45
	v_fmac_f32_e32 v32, v70, v45
	v_fmac_f32_e32 v33, v69, v45
	v_fmac_f32_e32 v34, v68, v45
	v_fmac_f32_e32 v35, v67, v45
	v_fmac_f32_e32 v36, v66, v45
	v_fmac_f32_e32 v37, v65, v45
	v_fmac_f32_e32 v38, v64, v45
	v_fmac_f32_e32 v39, v63, v45
	v_fmac_f32_e32 v40, v62, v45
	v_fmac_f32_e32 v41, v61, v45
	v_fmac_f32_e32 v42, v60, v45
	v_fmac_f32_e32 v43, v59, v45
	v_fmac_f32_e32 v44, v58, v45
	s_waitcnt lgkmcnt(7)
	v_lshlrev_b32_e32 v45, 16, v104
	ds_read_u16 v104, v22 offset:29696
	v_fmac_f32_e32 v29, v74, v45
	v_fmac_f32_e32 v30, v73, v45
	v_fmac_f32_e32 v31, v72, v45
	v_fmac_f32_e32 v32, v71, v45
	v_fmac_f32_e32 v33, v70, v45
	v_fmac_f32_e32 v34, v69, v45
	v_fmac_f32_e32 v35, v68, v45
	v_fmac_f32_e32 v36, v67, v45
	v_fmac_f32_e32 v37, v66, v45
	v_fmac_f32_e32 v38, v65, v45
	v_fmac_f32_e32 v39, v64, v45
	v_fmac_f32_e32 v40, v63, v45
	v_fmac_f32_e32 v41, v62, v45
	v_fmac_f32_e32 v42, v61, v45
	v_fmac_f32_e32 v43, v60, v45
	v_fmac_f32_e32 v44, v59, v45
	s_waitcnt lgkmcnt(7)
	v_lshlrev_b32_e32 v45, 16, v105
	ds_read_u16 v105, v22 offset:30720
	v_fmac_f32_e32 v29, v75, v45
	v_fmac_f32_e32 v30, v74, v45
	v_fmac_f32_e32 v31, v73, v45
	v_fmac_f32_e32 v32, v72, v45
	v_fmac_f32_e32 v33, v71, v45
	v_fmac_f32_e32 v34, v70, v45
	v_fmac_f32_e32 v35, v69, v45
	v_fmac_f32_e32 v36, v68, v45
	v_fmac_f32_e32 v37, v67, v45
	v_fmac_f32_e32 v38, v66, v45
	v_fmac_f32_e32 v39, v65, v45
	v_fmac_f32_e32 v40, v64, v45
	v_fmac_f32_e32 v41, v63, v45
	v_fmac_f32_e32 v42, v62, v45
	v_fmac_f32_e32 v43, v61, v45
	v_fmac_f32_e32 v44, v60, v45
	s_waitcnt lgkmcnt(7)
	v_lshlrev_b32_e32 v45, 16, v106
	ds_read_u16 v106, v22 offset:31744
	v_fmac_f32_e32 v29, v76, v45
	v_fmac_f32_e32 v30, v75, v45
	v_fmac_f32_e32 v31, v74, v45
	v_fmac_f32_e32 v32, v73, v45
	v_fmac_f32_e32 v33, v72, v45
	v_fmac_f32_e32 v34, v71, v45
	v_fmac_f32_e32 v35, v70, v45
	v_fmac_f32_e32 v36, v69, v45
	v_fmac_f32_e32 v37, v68, v45
	v_fmac_f32_e32 v38, v67, v45
	v_fmac_f32_e32 v39, v66, v45
	v_fmac_f32_e32 v40, v65, v45
	v_fmac_f32_e32 v41, v64, v45
	v_fmac_f32_e32 v42, v63, v45
	v_fmac_f32_e32 v43, v62, v45
	v_fmac_f32_e32 v44, v61, v45
	s_waitcnt lgkmcnt(7)
	v_lshlrev_b32_e32 v45, 16, v107
	ds_read_u16 v107, v22 offset:32768
	v_fmac_f32_e32 v29, v77, v45
	v_fmac_f32_e32 v30, v76, v45
	v_fmac_f32_e32 v31, v75, v45
	v_fmac_f32_e32 v32, v74, v45
	v_fmac_f32_e32 v33, v73, v45
	v_fmac_f32_e32 v34, v72, v45
	v_fmac_f32_e32 v35, v71, v45
	v_fmac_f32_e32 v36, v70, v45
	v_fmac_f32_e32 v37, v69, v45
	v_fmac_f32_e32 v38, v68, v45
	v_fmac_f32_e32 v39, v67, v45
	v_fmac_f32_e32 v40, v66, v45
	v_fmac_f32_e32 v41, v65, v45
	v_fmac_f32_e32 v42, v64, v45
	v_fmac_f32_e32 v43, v63, v45
	v_fmac_f32_e32 v44, v62, v45
	s_waitcnt lgkmcnt(7)
	v_lshlrev_b32_e32 v45, 16, v100
	ds_read_u16 v100, v22 offset:33792
	v_fmac_f32_e32 v29, v78, v45
	v_fmac_f32_e32 v30, v77, v45
	v_fmac_f32_e32 v31, v76, v45
	v_fmac_f32_e32 v32, v75, v45
	v_fmac_f32_e32 v33, v74, v45
	v_fmac_f32_e32 v34, v73, v45
	v_fmac_f32_e32 v35, v72, v45
	v_fmac_f32_e32 v36, v71, v45
	v_fmac_f32_e32 v37, v70, v45
	v_fmac_f32_e32 v38, v69, v45
	v_fmac_f32_e32 v39, v68, v45
	v_fmac_f32_e32 v40, v67, v45
	v_fmac_f32_e32 v41, v66, v45
	v_fmac_f32_e32 v42, v65, v45
	v_fmac_f32_e32 v43, v64, v45
	v_fmac_f32_e32 v44, v63, v45
	s_waitcnt lgkmcnt(7)
	v_lshlrev_b32_e32 v45, 16, v101
	ds_read_u16 v101, v22 offset:34816
	v_fmac_f32_e32 v29, v79, v45
	v_fmac_f32_e32 v30, v78, v45
	v_fmac_f32_e32 v31, v77, v45
	v_fmac_f32_e32 v32, v76, v45
	v_fmac_f32_e32 v33, v75, v45
	v_fmac_f32_e32 v34, v74, v45
	v_fmac_f32_e32 v35, v73, v45
	v_fmac_f32_e32 v36, v72, v45
	v_fmac_f32_e32 v37, v71, v45
	v_fmac_f32_e32 v38, v70, v45
	v_fmac_f32_e32 v39, v69, v45
	v_fmac_f32_e32 v40, v68, v45
	v_fmac_f32_e32 v41, v67, v45
	v_fmac_f32_e32 v42, v66, v45
	v_fmac_f32_e32 v43, v65, v45
	v_fmac_f32_e32 v44, v64, v45
	s_waitcnt lgkmcnt(7)
	v_lshlrev_b32_e32 v45, 16, v102
	ds_read_u16 v102, v22 offset:35840
	v_fmac_f32_e32 v29, v80, v45
	v_fmac_f32_e32 v30, v79, v45
	v_fmac_f32_e32 v31, v78, v45
	v_fmac_f32_e32 v32, v77, v45
	v_fmac_f32_e32 v33, v76, v45
	v_fmac_f32_e32 v34, v75, v45
	v_fmac_f32_e32 v35, v74, v45
	v_fmac_f32_e32 v36, v73, v45
	v_fmac_f32_e32 v37, v72, v45
	v_fmac_f32_e32 v38, v71, v45
	v_fmac_f32_e32 v39, v70, v45
	v_fmac_f32_e32 v40, v69, v45
	v_fmac_f32_e32 v41, v68, v45
	v_fmac_f32_e32 v42, v67, v45
	v_fmac_f32_e32 v43, v66, v45
	v_fmac_f32_e32 v44, v65, v45
	s_waitcnt lgkmcnt(7)
	v_lshlrev_b32_e32 v45, 16, v103
	ds_read_u16 v103, v22 offset:36864
	v_fmac_f32_e32 v29, v81, v45
	v_fmac_f32_e32 v30, v80, v45
	v_fmac_f32_e32 v31, v79, v45
	v_fmac_f32_e32 v32, v78, v45
	v_fmac_f32_e32 v33, v77, v45
	v_fmac_f32_e32 v34, v76, v45
	v_fmac_f32_e32 v35, v75, v45
	v_fmac_f32_e32 v36, v74, v45
	v_fmac_f32_e32 v37, v73, v45
	v_fmac_f32_e32 v38, v72, v45
	v_fmac_f32_e32 v39, v71, v45
	v_fmac_f32_e32 v40, v70, v45
	v_fmac_f32_e32 v41, v69, v45
	v_fmac_f32_e32 v42, v68, v45
	v_fmac_f32_e32 v43, v67, v45
	v_fmac_f32_e32 v44, v66, v45
	s_waitcnt lgkmcnt(7)
	v_lshlrev_b32_e32 v45, 16, v104
	ds_read_u16 v104, v22 offset:37888
	v_fmac_f32_e32 v29, v82, v45
	v_fmac_f32_e32 v30, v81, v45
	v_fmac_f32_e32 v31, v80, v45
	v_fmac_f32_e32 v32, v79, v45
	v_fmac_f32_e32 v33, v78, v45
	v_fmac_f32_e32 v34, v77, v45
	v_fmac_f32_e32 v35, v76, v45
	v_fmac_f32_e32 v36, v75, v45
	v_fmac_f32_e32 v37, v74, v45
	v_fmac_f32_e32 v38, v73, v45
	v_fmac_f32_e32 v39, v72, v45
	v_fmac_f32_e32 v40, v71, v45
	v_fmac_f32_e32 v41, v70, v45
	v_fmac_f32_e32 v42, v69, v45
	v_fmac_f32_e32 v43, v68, v45
	v_fmac_f32_e32 v44, v67, v45
	s_waitcnt lgkmcnt(7)
	v_lshlrev_b32_e32 v45, 16, v105
	ds_read_u16 v105, v22 offset:38912
	v_fmac_f32_e32 v29, v83, v45
	v_fmac_f32_e32 v30, v82, v45
	v_fmac_f32_e32 v31, v81, v45
	v_fmac_f32_e32 v32, v80, v45
	v_fmac_f32_e32 v33, v79, v45
	v_fmac_f32_e32 v34, v78, v45
	v_fmac_f32_e32 v35, v77, v45
	v_fmac_f32_e32 v36, v76, v45
	v_fmac_f32_e32 v37, v75, v45
	v_fmac_f32_e32 v38, v74, v45
	v_fmac_f32_e32 v39, v73, v45
	v_fmac_f32_e32 v40, v72, v45
	v_fmac_f32_e32 v41, v71, v45
	v_fmac_f32_e32 v42, v70, v45
	v_fmac_f32_e32 v43, v69, v45
	v_fmac_f32_e32 v44, v68, v45
	s_waitcnt lgkmcnt(7)
	v_lshlrev_b32_e32 v45, 16, v106
	ds_read_u16 v106, v22 offset:39936
	v_fmac_f32_e32 v30, v83, v45
	v_fmac_f32_e32 v31, v82, v45
	v_fmac_f32_e32 v32, v81, v45
	v_fmac_f32_e32 v33, v80, v45
	v_fmac_f32_e32 v34, v79, v45
	v_fmac_f32_e32 v35, v78, v45
	v_fmac_f32_e32 v36, v77, v45
	v_fmac_f32_e32 v37, v76, v45
	v_fmac_f32_e32 v38, v75, v45
	v_fmac_f32_e32 v39, v74, v45
	v_fmac_f32_e32 v40, v73, v45
	v_fmac_f32_e32 v41, v72, v45
	v_fmac_f32_e32 v42, v71, v45
	v_fmac_f32_e32 v43, v70, v45
	v_fmac_f32_e32 v44, v69, v45
	s_waitcnt lgkmcnt(7)
	v_lshlrev_b32_e32 v45, 16, v107
	ds_read_u16 v107, v22 offset:40960
	v_fmac_f32_e32 v31, v83, v45
	v_fmac_f32_e32 v32, v82, v45
	v_fmac_f32_e32 v33, v81, v45
	v_fmac_f32_e32 v34, v80, v45
	v_fmac_f32_e32 v35, v79, v45
	v_fmac_f32_e32 v36, v78, v45
	v_fmac_f32_e32 v37, v77, v45
	v_fmac_f32_e32 v38, v76, v45
	v_fmac_f32_e32 v39, v75, v45
	v_fmac_f32_e32 v40, v74, v45
	v_fmac_f32_e32 v41, v73, v45
	v_fmac_f32_e32 v42, v72, v45
	v_fmac_f32_e32 v43, v71, v45
	v_fmac_f32_e32 v44, v70, v45
	s_waitcnt lgkmcnt(7)
	v_lshlrev_b32_e32 v45, 16, v100
	ds_read_u16 v100, v22 offset:41984
	v_fmac_f32_e32 v32, v83, v45
	v_fmac_f32_e32 v33, v82, v45
	v_fmac_f32_e32 v34, v81, v45
	v_fmac_f32_e32 v35, v80, v45
	v_fmac_f32_e32 v36, v79, v45
	v_fmac_f32_e32 v37, v78, v45
	v_fmac_f32_e32 v38, v77, v45
	v_fmac_f32_e32 v39, v76, v45
	v_fmac_f32_e32 v40, v75, v45
	v_fmac_f32_e32 v41, v74, v45
	v_fmac_f32_e32 v42, v73, v45
	v_fmac_f32_e32 v43, v72, v45
	v_fmac_f32_e32 v44, v71, v45
	s_waitcnt lgkmcnt(7)
	v_lshlrev_b32_e32 v45, 16, v101
	ds_read_u16 v101, v22 offset:43008
	v_fmac_f32_e32 v33, v83, v45
	v_fmac_f32_e32 v34, v82, v45
	v_fmac_f32_e32 v35, v81, v45
	v_fmac_f32_e32 v36, v80, v45
	v_fmac_f32_e32 v37, v79, v45
	v_fmac_f32_e32 v38, v78, v45
	v_fmac_f32_e32 v39, v77, v45
	v_fmac_f32_e32 v40, v76, v45
	v_fmac_f32_e32 v41, v75, v45
	v_fmac_f32_e32 v42, v74, v45
	v_fmac_f32_e32 v43, v73, v45
	v_fmac_f32_e32 v44, v72, v45
	s_waitcnt lgkmcnt(7)
	v_lshlrev_b32_e32 v45, 16, v102
	ds_read_u16 v102, v22 offset:44032
	v_fmac_f32_e32 v34, v83, v45
	v_fmac_f32_e32 v35, v82, v45
	v_fmac_f32_e32 v36, v81, v45
	v_fmac_f32_e32 v37, v80, v45
	v_fmac_f32_e32 v38, v79, v45
	v_fmac_f32_e32 v39, v78, v45
	v_fmac_f32_e32 v40, v77, v45
	v_fmac_f32_e32 v41, v76, v45
	v_fmac_f32_e32 v42, v75, v45
	v_fmac_f32_e32 v43, v74, v45
	v_fmac_f32_e32 v44, v73, v45
	s_waitcnt lgkmcnt(7)
	v_lshlrev_b32_e32 v45, 16, v103
	ds_read_u16 v103, v22 offset:45056
	v_fmac_f32_e32 v35, v83, v45
	v_fmac_f32_e32 v36, v82, v45
	v_fmac_f32_e32 v37, v81, v45
	v_fmac_f32_e32 v38, v80, v45
	v_fmac_f32_e32 v39, v79, v45
	v_fmac_f32_e32 v40, v78, v45
	v_fmac_f32_e32 v41, v77, v45
	v_fmac_f32_e32 v42, v76, v45
	v_fmac_f32_e32 v43, v75, v45
	v_fmac_f32_e32 v44, v74, v45
	s_waitcnt lgkmcnt(7)
	v_lshlrev_b32_e32 v45, 16, v104
	ds_read_u16 v104, v22 offset:46080
	v_fmac_f32_e32 v36, v83, v45
	v_fmac_f32_e32 v37, v82, v45
	v_fmac_f32_e32 v38, v81, v45
	v_fmac_f32_e32 v39, v80, v45
	v_fmac_f32_e32 v40, v79, v45
	v_fmac_f32_e32 v41, v78, v45
	v_fmac_f32_e32 v42, v77, v45
	v_fmac_f32_e32 v43, v76, v45
	v_fmac_f32_e32 v44, v75, v45
	s_waitcnt lgkmcnt(7)
	v_lshlrev_b32_e32 v45, 16, v105
	v_fmac_f32_e32 v37, v83, v45
	v_fmac_f32_e32 v38, v82, v45
	v_fmac_f32_e32 v39, v81, v45
	v_fmac_f32_e32 v40, v80, v45
	v_fmac_f32_e32 v41, v79, v45
	v_fmac_f32_e32 v42, v78, v45
	v_fmac_f32_e32 v43, v77, v45
	v_fmac_f32_e32 v44, v76, v45
	s_waitcnt lgkmcnt(6)
	v_lshlrev_b32_e32 v45, 16, v106
	v_fmac_f32_e32 v38, v83, v45
	v_fmac_f32_e32 v39, v82, v45
	v_fmac_f32_e32 v40, v81, v45
	v_fmac_f32_e32 v41, v80, v45
	v_fmac_f32_e32 v42, v79, v45
	v_fmac_f32_e32 v43, v78, v45
	v_fmac_f32_e32 v44, v77, v45
	s_waitcnt lgkmcnt(5)
	v_lshlrev_b32_e32 v45, 16, v107
	v_fmac_f32_e32 v39, v83, v45
	v_fmac_f32_e32 v40, v82, v45
	v_fmac_f32_e32 v41, v81, v45
	v_fmac_f32_e32 v42, v80, v45
	v_fmac_f32_e32 v43, v79, v45
	v_fmac_f32_e32 v44, v78, v45
	s_waitcnt lgkmcnt(4)
	v_lshlrev_b32_e32 v45, 16, v100
	v_fmac_f32_e32 v40, v83, v45
	v_fmac_f32_e32 v41, v82, v45
	v_fmac_f32_e32 v42, v81, v45
	v_fmac_f32_e32 v43, v80, v45
	v_fmac_f32_e32 v44, v79, v45
	s_waitcnt lgkmcnt(3)
	v_lshlrev_b32_e32 v45, 16, v101
	v_fmac_f32_e32 v41, v83, v45
	v_fmac_f32_e32 v42, v82, v45
	v_fmac_f32_e32 v43, v81, v45
	v_fmac_f32_e32 v44, v80, v45
	s_waitcnt lgkmcnt(2)
	v_lshlrev_b32_e32 v45, 16, v102
	v_fmac_f32_e32 v42, v83, v45
	v_fmac_f32_e32 v43, v82, v45
	v_fmac_f32_e32 v44, v81, v45
	s_waitcnt lgkmcnt(1)
	v_lshlrev_b32_e32 v45, 16, v103
	v_fmac_f32_e32 v43, v83, v45
	v_fmac_f32_e32 v44, v82, v45
	s_waitcnt lgkmcnt(0)
	v_lshlrev_b32_e32 v45, 16, v104
	v_fmac_f32_e32 v44, v83, v45
	ds_write2st64_b32 v23, v29, v30 offset1:8
	ds_write2st64_b32 v23, v31, v32 offset0:16 offset1:24
	ds_write2st64_b32 v23, v33, v34 offset0:32 offset1:40
	ds_write2st64_b32 v23, v35, v36 offset0:48 offset1:56
	ds_write2st64_b32 v23, v37, v38 offset0:64 offset1:72
	ds_write2st64_b32 v23, v39, v40 offset0:80 offset1:88
	ds_write2st64_b32 v23, v41, v42 offset0:96 offset1:104
	ds_write2st64_b32 v23, v43, v44 offset0:112 offset1:120
	v_add_u32_e32 v29, s36, v24
	v_cmp_gt_i32_e32 vcc, 64, v29
	s_waitcnt vmcnt(0)
	s_waitcnt lgkmcnt(0)
	s_barrier
	s_and_saveexec_b64 s[34:35], vcc
	s_cbranch_execz .LBB0_2167
	ds_read_b128 v[30:33], v27
	ds_read_b128 v[34:37], v27 offset:16
	s_waitcnt lgkmcnt(1)
	v_mov_b32_e32 v38, v31
	v_mov_b32_e32 v39, v32
	v_mov_b32_e32 v40, v30
	v_mov_b32_e32 v41, v33
	v_pk_add_f32 v[38:39], v[38:39], v[40:41]
	s_waitcnt lgkmcnt(0)
	v_mov_b32_e32 v40, v36
	v_mov_b32_e32 v41, v34
	v_mov_b32_e32 v42, v37
	v_mov_b32_e32 v43, v35
	v_pk_add_f32 v[40:41], v[40:41], v[42:43]
	v_add_f32_e32 v29, v38, v39
	v_add_f32_e32 v29, v29, v41
	v_add_f32_e32 v29, v40, v29
	v_and_b32_e32 v39, 64, v214
	v_xor_b32_e32 v38, 16, v214
	v_add_f32_dpp v29, v29, v29 quad_perm:[1,0,3,2] row_mask:0xf bank_mask:0xf bound_ctrl:1
	v_add_u32_e32 v39, 64, v39
	v_cmp_lt_i32_e32 vcc, v38, v39
	v_add_f32_dpp v29, v29, v29 quad_perm:[2,3,0,1] row_mask:0xf bank_mask:0xf bound_ctrl:1
	s_nop 0
	v_cndmask_b32_e32 v38, v214, v38, vcc
	v_add_f32_dpp v29, v29, v29 row_half_mirror row_mask:0xf bank_mask:0xf bound_ctrl:1
	v_lshlrev_b32_e32 v46, 2, v38
	s_nop 0
	v_add_f32_dpp v29, v29, v29 row_mirror row_mask:0xf bank_mask:0xf bound_ctrl:1
	v_mov_b32_e32 v38, v29
	v_mov_b32_e32 v108, v29
	s_nop 1
	v_permlane16_swap_b32_e32 v38, v108
	v_add_f32_e32 v29, v38, v108
	v_xor_b32_e32 v38, 32, v214
	v_cmp_lt_i32_e32 vcc, v38, v39
	s_nop 1
	v_cndmask_b32_e32 v38, v214, v38, vcc
	v_lshlrev_b32_e32 v47, 2, v38
	v_mov_b32_e32 v38, v29
	v_mov_b32_e32 v108, v29
	s_nop 1
	v_permlane32_swap_b32_e32 v38, v108
	v_add_f32_e32 v29, v38, v108
	v_fmamk_f32 v31, v29, 0xbb000000, v31
	v_fmamk_f32 v30, v29, 0xbb000000, v30
	v_fmamk_f32 v33, v29, 0xbb000000, v33
	v_fmac_f32_e32 v32, 0xbb000000, v29
	v_pk_mul_f32 v[38:39], v[32:33], v[32:33]
	v_pk_mul_f32 v[40:41], v[30:31], v[30:31]
	v_fmamk_f32 v35, v29, 0xbb000000, v35
	v_fmamk_f32 v34, v29, 0xbb000000, v34
	v_fmamk_f32 v37, v29, 0xbb000000, v37
	v_fmac_f32_e32 v36, 0xbb000000, v29
	v_pk_mov_b32 v[42:43], v[40:41], v[38:39] op_sel:[1,0]
	v_mov_b32_e32 v41, v39
	v_pk_add_f32 v[38:39], v[42:43], v[40:41]
	v_pk_mul_f32 v[40:41], v[36:37], v[36:37]
	v_pk_mul_f32 v[42:43], v[34:35], v[34:35]
	v_mov_b32_e32 v44, v40
	v_mov_b32_e32 v45, v42
	v_mov_b32_e32 v42, v41
	v_pk_add_f32 v[40:41], v[44:45], v[42:43]
	v_add_f32_e32 v29, v38, v39
	v_add_f32_e32 v29, v41, v29
	v_add_f32_e32 v29, v40, v29
	s_nop 1
	v_add_f32_dpp v29, v29, v29 quad_perm:[1,0,3,2] row_mask:0xf bank_mask:0xf bound_ctrl:1
	s_nop 1
	v_add_f32_dpp v29, v29, v29 quad_perm:[2,3,0,1] row_mask:0xf bank_mask:0xf bound_ctrl:1
	s_nop 1
	v_add_f32_dpp v29, v29, v29 row_half_mirror row_mask:0xf bank_mask:0xf bound_ctrl:1
	s_nop 1
	v_add_f32_dpp v29, v29, v29 row_mirror row_mask:0xf bank_mask:0xf bound_ctrl:1
	v_mov_b32_e32 v38, v29
	v_mov_b32_e32 v108, v29
	s_nop 1
	v_permlane16_swap_b32_e32 v38, v108
	v_add_f32_e32 v29, v38, v108
	v_mov_b32_e32 v38, v29
	v_mov_b32_e32 v108, v29
	s_nop 1
	v_permlane32_swap_b32_e32 v38, v108
	v_add_f32_e32 v29, v38, v108
	v_fmamk_f32 v29, v29, 0x3b000000, v1
	v_mul_f32_e32 v38, 0x4b800000, v29
	v_cmp_gt_f32_e32 vcc, s77, v29
	s_nop 1
	v_cndmask_b32_e32 v29, v29, v38, vcc
	v_rsq_f32_e32 v29, v29
	s_nop 0
	v_mul_f32_e32 v38, 0x45800000, v29
	v_cndmask_b32_e32 v38, v29, v38, vcc
	v_pk_mul_f32 v[30:31], v[30:31], v[38:39] op_sel_hi:[1,0]
	v_pk_mul_f32 v[34:35], v[34:35], v[38:39] op_sel_hi:[1,0]
	v_pk_fma_f32 v[30:31], v[6:7], v[30:31], v[14:15]
	v_pk_fma_f32 v[34:35], v[2:3], v[34:35], v[10:11]
	v_mul_f32_e32 v29, 0xbfb8aa3b, v30
	v_pk_mul_f32 v[32:33], v[32:33], v[38:39] op_sel_hi:[1,0]
	v_pk_mul_f32 v[36:37], v[36:37], v[38:39] op_sel_hi:[1,0]
	v_exp_f32_e32 v29, v29
	v_mul_f32_e32 v38, 0xbfb8aa3b, v34
	v_exp_f32_e32 v39, v38
	v_mul_f32_e32 v40, 0xbfb8aa3b, v35
	v_add_f32_e32 v29, 1.0, v29
	v_rcp_f32_e32 v38, v29
	v_add_f32_e32 v29, 1.0, v39
	v_mul_f32_e32 v39, 0xbfb8aa3b, v31
	v_exp_f32_e32 v39, v39
	v_exp_f32_e32 v41, v40
	v_pk_fma_f32 v[32:33], v[8:9], v[32:33], v[16:17]
	v_rcp_f32_e32 v40, v29
	v_add_f32_e32 v29, 1.0, v39
	v_pk_fma_f32 v[36:37], v[4:5], v[36:37], v[12:13]
	v_rcp_f32_e32 v39, v29
	v_add_f32_e32 v29, 1.0, v41
	v_mul_f32_e32 v41, 0xbfb8aa3b, v32
	v_exp_f32_e32 v42, v41
	v_mul_f32_e32 v41, 0xbfb8aa3b, v36
	v_exp_f32_e32 v43, v41
	v_rcp_f32_e32 v41, v29
	v_add_f32_e32 v29, 1.0, v42
	v_rcp_f32_e32 v42, v29
	v_add_f32_e32 v29, 1.0, v43
	v_mul_f32_e32 v43, 0xbfb8aa3b, v33
	v_exp_f32_e32 v43, v43
	v_mul_f32_e32 v44, 0xbfb8aa3b, v37
	v_exp_f32_e32 v45, v44
	v_rcp_f32_e32 v44, v29
	v_add_f32_e32 v29, 1.0, v43
	v_rcp_f32_e32 v43, v29
	v_add_f32_e32 v29, 1.0, v45
	v_rcp_f32_e32 v45, v29
	v_pk_mul_f32 v[30:31], v[30:31], v[38:39]
	v_pk_mul_f32 v[34:35], v[34:35], v[40:41]
	v_pk_mul_f32 v[32:33], v[32:33], v[42:43]
	v_cvt_pk_bf16_f32 v30, v30, v31
	v_cvt_pk_bf16_f32 v31, v32, v33
	v_cvt_pk_bf16_f32 v32, v34, v35
	v_add_u32_e32 v34, s36, v26
	v_ashrrev_i32_e32 v35, 31, v34
	v_pk_mul_f32 v[36:37], v[36:37], v[44:45]
	v_lshlrev_b64 v[34:35], 11, v[34:35]
	v_cvt_pk_bf16_f32 v33, v36, v37
	v_lshl_add_u64 v[34:35], v[18:19], 0, v[34:35]
	global_store_dwordx4 v[34:35], v[30:33], off offset:1024
